# spatial-gating unit: mixing-matrix (tril) row loads beyond the wave's last output row are exec-masked (37 pct fewer 32-line load instructions); on top of K swizzle fix
# speedup vs baseline: 1.0078x; 1.0016x over previous
; __device__ __forceinline__ int crow(int r, int hi) { return (r & 3) + 8 * (r >> 2) + 4 * hi; }
; __device__ __forceinline__ void unit(const bf16_t* proj, const float* stats  , const float* lng, const float* lnb, const float* sw, const float* sb, bf16_t* Y2, int un, LAS unsigned char* lds) {
;     ...
;     f32x4 wv[16]; unsigned uu[32], zq[32]; float bias[16];
; #pragma unroll
;     for (int i = 0; i < 8; ++i) { const int s0 = (i >> 2) * 64 + 16 * (i & 3) + hi * 8; const float* wp = sw + ((size_t)g * 128 + t) * 128 + s0; wv[2 * i] = *(const f32x4*)wp; wv[2 * i + 1] = *(const f32x4*)(wp + 4); }
; #pragma unroll
;     for (int r = 0; r < 16; ++r) { const int tr = tb * 32 + att::crow(r, hi), bt = R0 + tr; bias[r] = sb[g * 128 + tr];
; #pragma unroll
;         for (int d = 0; d < 2; ++d) { const int ch = g * 128 + (2 * eh + d) * 32 + (r32 & ~1); uu[r * 2 + d] = *(const unsigned*)(proj + (size_t)bt * NC + C_UC + ch); zq[r * 2 + d] = *(const unsigned*)(proj + (size_t)bt * NC + C_ZC + ch); } }
.LBB0_1376:
	s_andn2_b64 vcc, exec, s[0:1]
	s_cbranch_vccnz .LBB0_425
	v_readlane_b32 s4, v252, 35
	v_readlane_b32 s10, v252, 41
	v_readlane_b32 s11, v252, 42
	s_mov_b64 s[0:1], s[10:11]
	v_readlane_b32 s5, v252, 36
	v_readlane_b32 s12, v252, 43
	v_readlane_b32 s13, v252, 44
	v_readlane_b32 s10, v254, 43
	v_readlane_b32 s11, v254, 44
	s_add_u32 s0, s0, s10
	s_mov_b64 s[4:5], s[12:13]
	s_addc_u32 s1, s1, s11
	v_readlane_b32 s6, v252, 37
	v_readlane_b32 s7, v252, 38
	v_readlane_b32 s8, v252, 39
	v_readlane_b32 s9, v252, 40
	v_readlane_b32 s14, v252, 45
	v_readlane_b32 s15, v252, 46
	s_add_u32 s4, s4, s10
	s_addc_u32 s5, s5, s11
	s_mov_b64 s[6:7], s[14:15]
	v_readlane_b32 s8, v253, 54
	v_readlane_b32 s16, v252, 47
	v_readlane_b32 s17, v252, 48
	v_readlane_b32 s9, v253, 55
	s_add_u32 s12, s6, s8
	s_addc_u32 s13, s7, s9
	s_mov_b64 s[6:7], s[16:17]
	s_add_u32 s6, s6, s10
	v_readlane_b32 s8, v254, 47
	s_addc_u32 s7, s7, s11
	s_waitcnt vmcnt(23)
	v_mov_b32_e32 v176, v0
	s_and_b32 s2, s8, 7
	s_lshl_b32 s8, s8, 4
	s_add_i32 s8, s8, 0x7fffe000
	v_readfirstlane_b32 s10, v176
	s_and_b32 s11, s8, 0x7fffff80
	s_lshr_b32 s8, s10, 1
	v_and_b32_e32 v177, 31, v176
	s_and_b32 s9, s8, 0x60
	v_or_b32_e32 v182, s9, v177
	s_lshl_b32 s8, s2, 16
	s_waitcnt vmcnt(3)
	v_lshl_or_b32 v2, v182, 9, s8
	v_lshl_add_u64 v[4:5], s[12:13], 0, v[2:3]
	v_and_b32_e32 v2, 32, v176
	s_lshl_b32 s2, s2, 7
	s_ashr_i32 s8, s10, 2
	v_lshl_add_u64 v[40:41], v[4:5], 0, v[2:3]
	s_andn2_b32 s8, s8, 63
	v_and_or_b32 v2, v176, 30, s2
	s_waitcnt vmcnt(0)
	v_bfe_u32 v1, v176, 5, 1
	v_add_u32_e32 v68, s8, v2
	v_readlane_b32 s12, v253, 48
	v_lshlrev_b32_e32 v183, 3, v1
	v_lshl_or_b32 v1, v1, 2, s9
	v_ashrrev_i32_e32 v69, 31, v68
	v_readlane_b32 s13, v253, 49
	v_or_b32_e32 v2, s11, v1
	s_mov_b32 s14, 0xe800
	v_mov_b64_e32 v[100:101], s[12:13]
	v_lshlrev_b64 v[84:85], 1, v[68:69]
	v_or_b32_e32 v68, 32, v68
	v_readlane_b32 s18, v252, 49
	v_readlane_b32 s19, v252, 50
	v_mad_u64_u32 v[70:71], s[12:13], v2, s14, v[100:101]
	s_mov_b64 s[16:17], 0x4000
	v_ashrrev_i32_e32 v69, 31, v68
	v_lshl_add_u64 v[72:73], v[70:71], 0, s[16:17]
	s_mov_b64 s[18:19], 0x5000
	v_lshlrev_b64 v[86:87], 1, v[68:69]
	v_lshl_add_u64 v[70:71], v[70:71], 0, s[18:19]
	v_lshl_add_u64 v[74:75], v[72:73], 0, v[84:85]
	v_lshl_add_u64 v[68:69], v[72:73], 0, v[86:87]
	global_load_dwordx4 v[28:31], v[40:41], off offset:16
	global_load_dwordx4 v[32:35], v[40:41], off
	global_load_dwordx4 v[20:23], v[40:41], off offset:80
	global_load_dwordx4 v[24:27], v[40:41], off offset:64
	s_cmp_ge_u32 s9, 32
	s_cselect_b64 exec, -1, 0
	global_load_dwordx4 v[12:15], v[40:41], off offset:144
	global_load_dwordx4 v[16:19], v[40:41], off offset:128
	s_waitcnt lgkmcnt(0)
	global_load_dwordx4 v[4:7], v[40:41], off offset:208
	global_load_dwordx4 v[8:11], v[40:41], off offset:192
	s_cmp_ge_u32 s9, 64
	s_cselect_b64 exec, -1, 0
	global_load_dwordx4 v[60:63], v[40:41], off offset:272
	global_load_dwordx4 v[64:67], v[40:41], off offset:256
	global_load_dwordx4 v[52:55], v[40:41], off offset:336
	global_load_dwordx4 v[56:59], v[40:41], off offset:320
	s_cmp_ge_u32 s9, 0x60
	s_cselect_b64 exec, -1, 0
	global_load_dwordx4 v[44:47], v[40:41], off offset:400
	global_load_dwordx4 v[48:51], v[40:41], off offset:384
	global_load_dwordx4 v[36:39], v[40:41], off offset:464
	s_nop 0
	global_load_dwordx4 v[40:43], v[40:41], off offset:448
	s_mov_b64 exec, -1
	v_or_b32_e32 v1, s2, v1
	global_load_dword v180, v[74:75], off
	global_load_dword v178, v[68:69], off
	v_lshl_add_u64 v[74:75], v[70:71], 0, v[84:85]
	v_lshl_add_u64 v[68:69], v[70:71], 0, v[86:87]
	global_load_dword v181, v[74:75], off
	global_load_dword v179, v[68:69], off
	v_or_b32_e32 v68, 1, v2
	v_mad_u64_u32 v[68:69], s[12:13], v68, s14, v[100:101]
	v_lshl_add_u64 v[70:71], v[68:69], 0, s[16:17]
	v_lshl_add_u64 v[68:69], v[68:69], 0, s[18:19]
	v_lshl_add_u64 v[72:73], v[70:71], 0, v[84:85]
	v_lshl_add_u64 v[70:71], v[70:71], 0, v[86:87]
	global_load_dword v173, v[72:73], off
	global_load_dword v172, v[70:71], off
	v_lshl_add_u64 v[72:73], v[68:69], 0, v[84:85]
	v_lshl_add_u64 v[68:69], v[68:69], 0, v[86:87]
	global_load_dword v174, v[68:69], off
	v_or_b32_e32 v68, 2, v2
	v_mad_u64_u32 v[68:69], s[12:13], v68, s14, v[100:101]
	v_lshl_add_u64 v[70:71], v[68:69], 0, s[16:17]
	global_load_dword v175, v[72:73], off
	v_lshl_add_u64 v[68:69], v[68:69], 0, s[18:19]
	v_lshl_add_u64 v[72:73], v[70:71], 0, v[84:85]
	v_lshl_add_u64 v[70:71], v[70:71], 0, v[86:87]
	global_load_dword v170, v[72:73], off
	global_load_dword v168, v[70:71], off
	v_lshl_add_u64 v[72:73], v[68:69], 0, v[84:85]
	v_lshl_add_u64 v[68:69], v[68:69], 0, v[86:87]
	global_load_dword v169, v[68:69], off
	v_or_b32_e32 v68, 3, v2
	v_mad_u64_u32 v[68:69], s[12:13], v68, s14, v[100:101]
	v_lshl_add_u64 v[70:71], v[68:69], 0, s[16:17]
	global_load_dword v171, v[72:73], off
	v_lshl_add_u64 v[68:69], v[68:69], 0, s[18:19]
	v_lshl_add_u64 v[72:73], v[70:71], 0, v[84:85]
	v_lshl_add_u64 v[70:71], v[70:71], 0, v[86:87]
	global_load_dword v165, v[72:73], off
	global_load_dword v164, v[70:71], off
	v_lshl_add_u64 v[72:73], v[68:69], 0, v[84:85]
	v_lshl_add_u64 v[68:69], v[68:69], 0, v[86:87]
	global_load_dword v166, v[68:69], off
	v_or_b32_e32 v68, 8, v2
	v_mad_u64_u32 v[68:69], s[12:13], v68, s14, v[100:101]
	v_lshl_add_u64 v[70:71], v[68:69], 0, s[16:17]
	global_load_dword v167, v[72:73], off
	v_lshl_add_u64 v[68:69], v[68:69], 0, s[18:19]
	v_lshl_add_u64 v[72:73], v[70:71], 0, v[84:85]
	v_lshl_add_u64 v[70:71], v[70:71], 0, v[86:87]
	global_load_dword v162, v[72:73], off
	global_load_dword v160, v[70:71], off
	v_lshl_add_u64 v[72:73], v[68:69], 0, v[84:85]
; __device__ __forceinline__ int crow(int r, int hi) { return (r & 3) + 8 * (r >> 2) + 4 * hi; }
; __device__ __forceinline__ void unit(const bf16_t* proj, const float* stats  , const float* lng, const float* lnb, const float* sw, const float* sb, bf16_t* Y2, int un, LAS unsigned char* lds) {
;     ...
;     for (int r = 0; r < 16; ++r) { const int tr = tb * 32 + att::crow(r, hi), bt = R0 + tr; bias[r] = sb[g * 128 + tr];
; #pragma unroll
;         for (int d = 0; d < 2; ++d) { const int ch = g * 128 + (2 * eh + d) * 32 + (r32 & ~1); uu[r * 2 + d] = *(const unsigned*)(proj + (size_t)bt * NC + C_UC + ch); zq[r * 2 + d] = *(const unsigned*)(proj + (size_t)bt * NC + C_ZC + ch); } }
	v_lshl_add_u64 v[68:69], v[68:69], 0, v[86:87]
	global_load_dword v161, v[68:69], off
	v_or_b32_e32 v68, 9, v2
	v_mad_u64_u32 v[68:69], s[12:13], v68, s14, v[100:101]
	v_lshl_add_u64 v[70:71], v[68:69], 0, s[16:17]
	global_load_dword v163, v[72:73], off
	v_lshl_add_u64 v[68:69], v[68:69], 0, s[18:19]
	v_lshl_add_u64 v[72:73], v[70:71], 0, v[84:85]
	v_lshl_add_u64 v[70:71], v[70:71], 0, v[86:87]
	global_load_dword v157, v[72:73], off
	global_load_dword v156, v[70:71], off
	v_lshl_add_u64 v[72:73], v[68:69], 0, v[84:85]
	v_lshl_add_u64 v[68:69], v[68:69], 0, v[86:87]
	global_load_dword v158, v[68:69], off
	v_or_b32_e32 v68, 10, v2
	v_mad_u64_u32 v[68:69], s[12:13], v68, s14, v[100:101]
	v_lshl_add_u64 v[70:71], v[68:69], 0, s[16:17]
	global_load_dword v159, v[72:73], off
	v_lshl_add_u64 v[68:69], v[68:69], 0, s[18:19]
	v_lshl_add_u64 v[72:73], v[70:71], 0, v[84:85]
	v_lshl_add_u64 v[70:71], v[70:71], 0, v[86:87]
	global_load_dword v154, v[72:73], off
	global_load_dword v152, v[70:71], off
	v_lshl_add_u64 v[72:73], v[68:69], 0, v[84:85]
	v_lshl_add_u64 v[68:69], v[68:69], 0, v[86:87]
	global_load_dword v153, v[68:69], off
	v_or_b32_e32 v68, 11, v2
	v_mad_u64_u32 v[68:69], s[12:13], v68, s14, v[100:101]
	v_lshl_add_u64 v[70:71], v[68:69], 0, s[16:17]
	global_load_dword v155, v[72:73], off
	v_lshl_add_u64 v[68:69], v[68:69], 0, s[18:19]
	v_lshl_add_u64 v[72:73], v[70:71], 0, v[84:85]
	v_lshl_add_u64 v[70:71], v[70:71], 0, v[86:87]
	global_load_dword v149, v[72:73], off
	global_load_dword v148, v[70:71], off
	v_lshl_add_u64 v[72:73], v[68:69], 0, v[84:85]
	v_lshl_add_u64 v[68:69], v[68:69], 0, v[86:87]
	global_load_dword v150, v[68:69], off
	v_or_b32_e32 v68, 16, v2
	v_mad_u64_u32 v[68:69], s[12:13], v68, s14, v[100:101]
	v_lshl_add_u64 v[70:71], v[68:69], 0, s[16:17]
	v_lshl_add_u64 v[68:69], v[68:69], 0, s[18:19]
	v_lshl_add_u64 v[88:89], v[70:71], 0, v[84:85]
	global_load_dword v151, v[72:73], off
	global_load_dword v146, v[88:89], off
	v_lshl_add_u64 v[88:89], v[68:69], 0, v[84:85]
	v_lshl_add_u64 v[70:71], v[70:71], 0, v[86:87]
	v_lshl_add_u64 v[68:69], v[68:69], 0, v[86:87]
	global_load_dword v143, v[70:71], off
	global_load_dword v144, v[68:69], off
	v_or_b32_e32 v68, 17, v2
	v_mad_u64_u32 v[68:69], s[12:13], v68, s14, v[100:101]
	v_lshl_add_u64 v[70:71], v[68:69], 0, s[16:17]
	global_load_dword v147, v[88:89], off
	v_lshl_add_u64 v[68:69], v[68:69], 0, s[18:19]
	v_lshl_add_u64 v[88:89], v[70:71], 0, v[84:85]
	v_lshl_add_u64 v[70:71], v[70:71], 0, v[86:87]
	global_load_dword v140, v[88:89], off
	global_load_dword v139, v[70:71], off
	v_lshl_add_u64 v[88:89], v[68:69], 0, v[84:85]
	v_lshl_add_u64 v[68:69], v[68:69], 0, v[86:87]
	global_load_dword v141, v[68:69], off
	v_or_b32_e32 v68, 18, v2
	v_mad_u64_u32 v[68:69], s[12:13], v68, s14, v[100:101]
	v_lshl_add_u64 v[70:71], v[68:69], 0, s[16:17]
	global_load_dword v142, v[88:89], off
	v_lshl_add_u64 v[68:69], v[68:69], 0, s[18:19]
	v_lshl_add_u64 v[88:89], v[70:71], 0, v[84:85]
	v_lshl_add_u64 v[70:71], v[70:71], 0, v[86:87]
	global_load_dword v137, v[88:89], off
	global_load_dword v135, v[70:71], off
	v_lshl_add_u64 v[88:89], v[68:69], 0, v[84:85]
	v_lshl_add_u64 v[68:69], v[68:69], 0, v[86:87]
	global_load_dword v136, v[68:69], off
	v_or_b32_e32 v68, 19, v2
	v_mad_u64_u32 v[68:69], s[12:13], v68, s14, v[100:101]
	v_lshl_add_u64 v[70:71], v[68:69], 0, s[16:17]
	global_load_dword v138, v[88:89], off
	v_lshl_add_u64 v[68:69], v[68:69], 0, s[18:19]
	v_lshl_add_u64 v[88:89], v[70:71], 0, v[84:85]
	v_lshl_add_u64 v[70:71], v[70:71], 0, v[86:87]
	global_load_dword v133, v[88:89], off
	global_load_dword v131, v[70:71], off
	v_lshl_add_u64 v[88:89], v[68:69], 0, v[84:85]
	v_lshlrev_b32_e32 v1, 2, v1
	global_load_dword v134, v[88:89], off
	v_lshl_add_u64 v[68:69], v[68:69], 0, v[86:87]
	v_or_b32_e32 v88, 24, v2
	global_load_dwordx4 v[80:83], v1, s[6:7]
	global_load_dwordx4 v[76:79], v1, s[6:7] offset:32
	global_load_dwordx4 v[72:75], v1, s[6:7] offset:64
	global_load_dword v132, v[68:69], off
	v_ashrrev_i32_e32 v185, 4, v176
	global_load_dwordx4 v[68:71], v1, s[6:7] offset:96
	v_mad_u64_u32 v[88:89], s[6:7], v88, s14, v[100:101]
	v_lshl_add_u64 v[90:91], v[88:89], 0, s[16:17]
	v_lshl_add_u64 v[88:89], v[88:89], 0, s[18:19]
	v_lshl_add_u64 v[92:93], v[90:91], 0, v[84:85]
	v_lshl_add_u64 v[90:91], v[90:91], 0, v[86:87]
	global_load_dword v129, v[92:93], off
	global_load_dword v127, v[90:91], off
	v_lshl_add_u64 v[92:93], v[88:89], 0, v[84:85]
	v_lshl_add_u64 v[88:89], v[88:89], 0, v[86:87]
	v_or_b32_e32 v1, 25, v2
	global_load_dword v128, v[88:89], off
	v_mad_u64_u32 v[88:89], s[6:7], v1, s14, v[100:101]
	v_lshl_add_u64 v[90:91], v[88:89], 0, s[16:17]
	global_load_dword v130, v[92:93], off
	v_lshl_add_u64 v[88:89], v[88:89], 0, s[18:19]
	v_lshl_add_u64 v[92:93], v[90:91], 0, v[84:85]
	v_lshl_add_u64 v[90:91], v[90:91], 0, v[86:87]
	global_load_dword v125, v[92:93], off
	global_load_dword v123, v[90:91], off
	v_lshl_add_u64 v[92:93], v[88:89], 0, v[84:85]
	v_lshl_add_u64 v[88:89], v[88:89], 0, v[86:87]
	v_or_b32_e32 v1, 26, v2
	global_load_dword v124, v[88:89], off
	v_mad_u64_u32 v[88:89], s[6:7], v1, s14, v[100:101]
	v_lshl_add_u64 v[90:91], v[88:89], 0, s[16:17]
	global_load_dword v126, v[92:93], off
	v_lshl_add_u64 v[88:89], v[88:89], 0, s[18:19]
	v_lshl_add_u64 v[92:93], v[90:91], 0, v[84:85]
	v_lshl_add_u64 v[90:91], v[90:91], 0, v[86:87]
	global_load_dword v121, v[92:93], off
	global_load_dword v119, v[90:91], off
	v_lshl_add_u64 v[92:93], v[88:89], 0, v[84:85]
	v_lshl_add_u64 v[88:89], v[88:89], 0, v[86:87]
	v_or_b32_e32 v1, 27, v2
	global_load_dword v120, v[88:89], off
; __device__ __forceinline__ void unit(const bf16_t* proj, const float* stats  , const float* lng, const float* lnb, const float* sw, const float* sb, bf16_t* Y2, int un, LAS unsigned char* lds) {
;     ...
;     { const int sr = tid >> 4, sc = (tid & 15) * 8, ch = g * 128 + sc;
;       const f32x4 g0 = *(const f32x4*)(lng + ch), g1 = *(const f32x4*)(lng + ch + 4), b0 = *(const f32x4*)(lnb + ch), b1 = *(const f32x4*)(lnb + ch + 4);
;       float mus[4], rss[4];
;       { float2 pp[4];
; #pragma unroll
;         for (int q = 0; q < 4; ++q) pp[q] = *(const float2*)(stats + ((size_t)(R0 + sr + 32 * q) * 16 + (tid & 15)) * 2);
;         asm volatile("" ::: "memory");
; #pragma unroll
;         for (int q = 0; q < 4; ++q) { float s1 = pp[q].x, s2 = pp[q].y;
; #pragma unroll
;             for (int off = 1; off < 16; off <<= 1) { s1 += __shfl_xor(s1, off); s2 += __shfl_xor(s2, off); }
;             mus[q] = s1 * (1.0f / 1024.0f); rss[q] = __builtin_amdgcn_rsqf(fmaxf(s2 * (1.0f / 1024.0f) - mus[q] * mus[q], 0.f) + LN_EPS); } }
	v_mad_u64_u32 v[88:89], s[6:7], v1, s14, v[100:101]
	v_lshl_add_u64 v[90:91], v[88:89], 0, s[16:17]
	v_lshl_add_u64 v[88:89], v[88:89], 0, s[18:19]
	global_load_dword v122, v[92:93], off
	v_lshl_add_u64 v[92:93], v[90:91], 0, v[84:85]
	v_lshl_add_u64 v[84:85], v[88:89], 0, v[84:85]
	global_load_dword v109, v[92:93], off
	global_load_dword v115, v[84:85], off
	v_lshl_add_u64 v[84:85], v[90:91], 0, v[86:87]
	global_load_dword v1, v[84:85], off
	v_lshl_add_u64 v[84:85], v[88:89], 0, v[86:87]
	global_load_dword v107, v[84:85], off
	v_and_b32_e32 v84, 15, v176
	v_lshlrev_b32_e32 v102, 3, v84
	v_or_b32_e32 v191, s2, v102
	v_lshlrev_b32_e32 v96, 2, v191
	global_load_dwordx4 v[84:87], v96, s[0:1] offset:16
	global_load_dwordx4 v[92:95], v96, s[0:1]
	global_load_dwordx4 v[88:91], v96, s[4:5] offset:16
	s_nop 0
	global_load_dwordx4 v[96:99], v96, s[4:5]
	v_add_u32_e32 v110, s11, v185
	v_readlane_b32 s0, v254, 37
	v_mov_b32_e32 v103, v3
	v_readlane_b32 s1, v254, 38
	v_ashrrev_i32_e32 v111, 31, v110
	v_lshlrev_b64 v[104:105], 7, v[110:111]
	v_lshl_add_u64 v[102:103], s[0:1], 0, v[102:103]
	v_lshl_add_u64 v[112:113], v[102:103], 0, v[104:105]
	global_load_dwordx2 v[104:105], v[112:113], off
	s_movk_i32 s0, 0x2000
	v_add_co_u32_e32 v116, vcc, s0, v112
	s_movk_i32 s0, 0x3000
	s_nop 0
	v_addc_co_u32_e32 v117, vcc, 0, v113, vcc
	global_load_dwordx2 v[102:103], v[116:117], off offset:-4096
	global_load_dwordx2 v[186:187], v[116:117], off
	v_add_co_u32_e32 v112, vcc, s0, v112
	v_and_b32_e32 v106, 64, v229
	s_nop 0
	v_addc_co_u32_e32 v113, vcc, 0, v113, vcc
	v_add_u32_e32 v106, 64, v106
	v_xor_b32_e32 v108, 1, v229
	v_cmp_lt_i32_e32 vcc, v108, v106
	global_load_dwordx2 v[188:189], v[112:113], off
	s_mov_b32 s0, 0x3a800000
	v_cndmask_b32_e32 v108, v229, v108, vcc
	v_lshlrev_b32_e32 v145, 2, v108
	v_xor_b32_e32 v108, 2, v229
	v_cmp_lt_i32_e32 vcc, v108, v106
	s_movk_i32 s4, 0x4000
	v_and_b32_e32 v184, 63, v176
	v_cndmask_b32_e32 v108, v229, v108, vcc
	v_lshlrev_b32_e32 v111, 2, v108
	v_xor_b32_e32 v108, 4, v229
	v_cmp_lt_i32_e32 vcc, v108, v106
	s_cmpk_gt_u32 s10, 0xff
	s_waitcnt vmcnt(3)
	ds_bpermute_b32 v112, v145, v104
	ds_bpermute_b32 v113, v145, v105
	v_cndmask_b32_e32 v108, v229, v108, vcc
	v_lshlrev_b32_e32 v190, 2, v108
	v_xor_b32_e32 v108, 8, v229
	v_cmp_lt_i32_e32 vcc, v108, v106
	s_waitcnt lgkmcnt(0)
	v_pk_add_f32 v[104:105], v[104:105], v[112:113]
	ds_bpermute_b32 v112, v111, v104
	ds_bpermute_b32 v113, v111, v105
	v_cndmask_b32_e32 v106, v229, v108, vcc
	v_lshlrev_b32_e32 v106, 2, v106
	s_waitcnt lgkmcnt(0)
	v_pk_add_f32 v[104:105], v[104:105], v[112:113]
	ds_bpermute_b32 v112, v190, v104
	ds_bpermute_b32 v113, v190, v105
	s_waitcnt lgkmcnt(0)
	v_pk_add_f32 v[104:105], v[104:105], v[112:113]
	ds_bpermute_b32 v112, v106, v104
	ds_bpermute_b32 v113, v106, v105
	s_waitcnt lgkmcnt(0)
	v_pk_add_f32 v[104:105], v[104:105], v[112:113]
	s_nop 0
	v_pk_mul_f32 v[116:117], v[104:105], s[0:1] op_sel_hi:[1,0]
	s_waitcnt vmcnt(2)
	ds_bpermute_b32 v105, v145, v103
	v_fma_f32 v104, -v116, v116, v117
	v_max_f32_e32 v104, 0, v104
	v_add_f32_e32 v104, 0x3727c5ac, v104
	v_rsq_f32_e32 v118, v104
	ds_bpermute_b32 v104, v145, v102
	s_waitcnt lgkmcnt(0)
	v_pk_add_f32 v[102:103], v[102:103], v[104:105]
	ds_bpermute_b32 v104, v111, v102
	ds_bpermute_b32 v105, v111, v103
	s_waitcnt lgkmcnt(0)
	v_pk_add_f32 v[102:103], v[102:103], v[104:105]
	ds_bpermute_b32 v104, v190, v102
	ds_bpermute_b32 v105, v190, v103
	s_waitcnt lgkmcnt(0)
	v_pk_add_f32 v[102:103], v[102:103], v[104:105]
	ds_bpermute_b32 v104, v106, v102
	ds_bpermute_b32 v105, v106, v103
	s_waitcnt lgkmcnt(0)
	v_pk_add_f32 v[102:103], v[102:103], v[104:105]
	s_nop 0
	v_pk_mul_f32 v[112:113], v[102:103], s[0:1] op_sel_hi:[1,0]
	s_waitcnt vmcnt(1)
	ds_bpermute_b32 v103, v145, v187
	v_fma_f32 v102, -v112, v112, v113
	v_max_f32_e32 v102, 0, v102
	v_add_f32_e32 v102, 0x3727c5ac, v102
	v_rsq_f32_e32 v114, v102
	ds_bpermute_b32 v102, v145, v186
	s_waitcnt lgkmcnt(0)
	v_pk_add_f32 v[102:103], v[186:187], v[102:103]
	ds_bpermute_b32 v104, v111, v102
	ds_bpermute_b32 v105, v111, v103
	s_waitcnt lgkmcnt(0)
	v_pk_add_f32 v[102:103], v[102:103], v[104:105]
	ds_bpermute_b32 v104, v190, v102
	ds_bpermute_b32 v105, v190, v103
	s_waitcnt lgkmcnt(0)
	v_pk_add_f32 v[102:103], v[102:103], v[104:105]
	ds_bpermute_b32 v104, v106, v102
	ds_bpermute_b32 v105, v106, v103
	s_waitcnt lgkmcnt(0)
	v_pk_add_f32 v[102:103], v[102:103], v[104:105]
	s_nop 0
	v_pk_mul_f32 v[102:103], v[102:103], s[0:1] op_sel_hi:[1,0]
	s_waitcnt vmcnt(0)
	ds_bpermute_b32 v105, v145, v189
	v_fma_f32 v104, -v102, v102, v103
	v_max_f32_e32 v104, 0, v104
	v_add_f32_e32 v104, 0x3727c5ac, v104
	v_rsq_f32_e32 v108, v104
	ds_bpermute_b32 v104, v145, v188
	s_waitcnt lgkmcnt(0)
	v_pk_add_f32 v[104:105], v[188:189], v[104:105]
	ds_bpermute_b32 v186, v111, v104
	ds_bpermute_b32 v187, v111, v105
	v_lshlrev_b32_e32 v111, 1, v185
	v_bfe_u32 v188, v176, 2, 2
	s_waitcnt lgkmcnt(0)
	v_pk_add_f32 v[104:105], v[104:105], v[186:187]
	ds_bpermute_b32 v186, v190, v104
	ds_bpermute_b32 v187, v190, v105
	s_waitcnt lgkmcnt(0)
	v_pk_add_f32 v[104:105], v[104:105], v[186:187]
	ds_bpermute_b32 v186, v106, v104
	ds_bpermute_b32 v187, v106, v105
	s_waitcnt lgkmcnt(0)
	v_pk_add_f32 v[104:105], v[104:105], v[186:187]
	v_and_b32_e32 v187, 8, v111
	v_lshrrev_b32_e32 v111, 1, v185
	v_and_b32_e32 v186, 3, v185
	v_and_or_b32 v111, v111, 4, v186
	v_pk_mul_f32 v[104:105], v[104:105], s[0:1] op_sel_hi:[1,0]
	v_lshlrev_b32_e32 v189, 6, v111
	v_mad_i64_i32 v[192:193], s[0:1], v110, s14, v[100:101]
	v_lshlrev_b32_e32 v110, 1, v191
	v_mov_b32_e32 v111, v3
	v_lshl_add_u64 v[192:193], v[192:193], 0, v[110:111]
	v_add_co_u32_e32 v192, vcc, s4, v192
	v_lshlrev_b32_e32 v186, 4, v176
	s_nop 0
	v_addc_co_u32_e32 v193, vcc, 0, v193, vcc
	global_load_dwordx4 v[196:199], v[192:193], off offset:2048
	v_and_b32_e32 v190, 48, v186
	v_fma_f32 v106, -v104, v104, v105
	v_max_f32_e32 v106, 0, v106
	v_add_f32_e32 v106, 0x3727c5ac, v106
	v_rsq_f32_e32 v106, v106
	s_waitcnt vmcnt(0)
; __device__ __forceinline__ unsigned cvt_pk_bf16(float lo, float hi) { f32x2_t v = {lo, hi}; bf16x2_t b = __builtin_convertvector(v, bf16x2_t); return __builtin_bit_cast(unsigned, b); }
; #define LAS __attribute__((address_space(3)))
; __device__ __forceinline__ float bflo(unsigned w) { return __uint_as_float(w << 16); }
; __device__ __forceinline__ float bfhi(unsigned w) { return __uint_as_float(w & 0xffff0000u); }
; __device__ __forceinline__ int v_st(int k, int c) { const int kk = (k & ~0xC) | ((k & 4) << 1) | ((k & 8) >> 1); return ((kk >> 3) * 4 + (c >> 5)) * 512 + ((kk & 7) * 32 + (c & 31)) * 2; }
; __device__ __forceinline__ void unit(const bf16_t* proj, const float* stats  , const float* lng, const float* lnb, const float* sw, const float* sb, bf16_t* Y2, int un, LAS unsigned char* lds) {
;     ...
;       for (int q = 0; q < 4; ++q) { const int s = sr + 32 * q, row = R0 + s; const u32x4 vv = *(const u32x4*)(proj + (size_t)row * NC + C_VC + ch);
;           const float mu = mus[q], rs = rss[q];
;           u32x4 w; w.x = pg8::cvt_pk_bf16((bflo(vv.x) - mu) * rs * g0[0] + b0[0], (bfhi(vv.x) - mu) * rs * g0[1] + b0[1]); w.y = pg8::cvt_pk_bf16((bflo(vv.y) - mu) * rs * g0[2] + b0[2], (bfhi(vv.y) - mu) * rs * g0[3] + b0[3]);
;           w.z = pg8::cvt_pk_bf16((bflo(vv.z) - mu) * rs * g1[0] + b1[0], (bfhi(vv.z) - mu) * rs * g1[1] + b1[1]); w.w = pg8::cvt_pk_bf16((bflo(vv.w) - mu) * rs * g1[2] + b1[2], (bfhi(vv.w) - mu) * rs * g1[3] + b1[3]);
;           *(LAS u32x4*)(lds + (s >> 6) * att::SHM_V + att::v_st(s & 63, sc)) = w; } }
	v_lshlrev_b32_e32 v192, 16, v196
	v_and_b32_e32 v193, 0xffff0000, v196
	v_pk_add_f32 v[192:193], v[192:193], v[116:117] op_sel_hi:[1,0] neg_lo:[0,1] neg_hi:[0,1]
	s_nop 0
	v_pk_mul_f32 v[192:193], v[118:119], v[192:193] op_sel_hi:[0,1]
	v_pk_fma_f32 v[192:193], v[92:93], v[192:193], v[96:97]
	s_nop 0
	v_cvt_pk_bf16_f32 v196, v192, v193
	v_lshlrev_b32_e32 v192, 16, v197
	v_and_b32_e32 v193, 0xffff0000, v197
	v_pk_add_f32 v[192:193], v[192:193], v[116:117] op_sel_hi:[1,0] neg_lo:[0,1] neg_hi:[0,1]
	s_nop 0
	v_pk_mul_f32 v[192:193], v[118:119], v[192:193] op_sel_hi:[0,1]
	v_pk_fma_f32 v[192:193], v[94:95], v[192:193], v[98:99]
	s_nop 0
	v_cvt_pk_bf16_f32 v197, v192, v193
	v_lshlrev_b32_e32 v192, 16, v198
	v_and_b32_e32 v193, 0xffff0000, v198
	v_pk_add_f32 v[192:193], v[192:193], v[116:117] op_sel_hi:[1,0] neg_lo:[0,1] neg_hi:[0,1]
	s_nop 0
	v_pk_mul_f32 v[192:193], v[118:119], v[192:193] op_sel_hi:[0,1]
	v_pk_fma_f32 v[192:193], v[84:85], v[192:193], v[88:89]
	s_nop 0
	v_cvt_pk_bf16_f32 v198, v192, v193
	v_lshlrev_b32_e32 v192, 16, v199
	v_and_b32_e32 v193, 0xffff0000, v199
	v_pk_add_f32 v[116:117], v[192:193], v[116:117] op_sel_hi:[1,0] neg_lo:[0,1] neg_hi:[0,1]
	s_nop 0
	v_pk_mul_f32 v[116:117], v[118:119], v[116:117] op_sel_hi:[0,1]
	v_pk_fma_f32 v[116:117], v[86:87], v[116:117], v[90:91]
	s_nop 0
	v_cvt_pk_bf16_f32 v199, v116, v117
	v_lshlrev_b32_e32 v116, 8, v185
	v_and_b32_e32 v117, 0xffffc000, v116
	v_and_or_b32 v116, v185, 48, v187
	v_lshrrev_b32_e32 v116, 1, v116
	v_or_b32_e32 v116, v116, v188
	v_lshlrev_b32_e32 v116, 9, v116
	v_add3_u32 v117, 0, v117, v116
	v_add3_u32 v117, v117, v189, v190
	ds_write_b128 v117, v[196:199]
	v_add_u32_e32 v117, 32, v185
	v_add_u32_e32 v118, s11, v117
	v_mad_i64_i32 v[192:193], s[0:1], v118, s14, v[100:101]
	v_lshl_add_u64 v[192:193], v[192:193], 0, v[110:111]
	v_add_co_u32_e32 v192, vcc, s4, v192
	s_nop 1
	v_addc_co_u32_e32 v193, vcc, 0, v193, vcc
	global_load_dwordx4 v[196:199], v[192:193], off offset:2048
	s_waitcnt vmcnt(0)
	v_lshlrev_b32_e32 v192, 16, v196
	v_and_b32_e32 v193, 0xffff0000, v196
	v_pk_add_f32 v[192:193], v[192:193], v[112:113] op_sel_hi:[1,0] neg_lo:[0,1] neg_hi:[0,1]
	s_nop 0
	v_pk_mul_f32 v[192:193], v[114:115], v[192:193] op_sel_hi:[0,1]
	v_pk_fma_f32 v[192:193], v[92:93], v[192:193], v[96:97]
	s_nop 0
	v_cvt_pk_bf16_f32 v196, v192, v193
	v_lshlrev_b32_e32 v192, 16, v197
	v_and_b32_e32 v193, 0xffff0000, v197
	v_pk_add_f32 v[192:193], v[192:193], v[112:113] op_sel_hi:[1,0] neg_lo:[0,1] neg_hi:[0,1]
	s_nop 0
	v_pk_mul_f32 v[192:193], v[114:115], v[192:193] op_sel_hi:[0,1]
	v_pk_fma_f32 v[192:193], v[94:95], v[192:193], v[98:99]
	s_nop 0
	v_cvt_pk_bf16_f32 v197, v192, v193
	v_lshlrev_b32_e32 v192, 16, v198
	v_and_b32_e32 v193, 0xffff0000, v198
	v_pk_add_f32 v[192:193], v[192:193], v[112:113] op_sel_hi:[1,0] neg_lo:[0,1] neg_hi:[0,1]
	s_nop 0
	v_pk_mul_f32 v[192:193], v[114:115], v[192:193] op_sel_hi:[0,1]
	v_pk_fma_f32 v[192:193], v[84:85], v[192:193], v[88:89]
	s_nop 0
	v_cvt_pk_bf16_f32 v198, v192, v193
	v_lshlrev_b32_e32 v192, 16, v199
	v_and_b32_e32 v193, 0xffff0000, v199
	v_pk_add_f32 v[112:113], v[192:193], v[112:113] op_sel_hi:[1,0] neg_lo:[0,1] neg_hi:[0,1]
	s_nop 0
	v_pk_mul_f32 v[112:113], v[114:115], v[112:113] op_sel_hi:[0,1]
	v_pk_fma_f32 v[112:113], v[86:87], v[112:113], v[90:91]
	v_add_u32_e32 v114, 64, v185
	v_cvt_pk_bf16_f32 v199, v112, v113
	v_and_or_b32 v113, v117, 48, v187
	v_lshrrev_b32_e32 v113, 1, v113
	v_lshlrev_b32_e32 v112, 8, v117
	v_or_b32_e32 v113, v113, v188
	v_and_b32_e32 v112, 0xffffc000, v112
	v_lshlrev_b32_e32 v113, 9, v113
	v_add3_u32 v112, 0, v112, v113
	v_add3_u32 v112, v112, v189, v190
	ds_write_b128 v112, v[196:199]
	v_add_u32_e32 v112, s11, v114
	v_mad_i64_i32 v[112:113], s[0:1], v112, s14, v[100:101]
	v_lshl_add_u64 v[112:113], v[112:113], 0, v[110:111]
	v_add_co_u32_e32 v112, vcc, s4, v112
	s_nop 1
	v_addc_co_u32_e32 v113, vcc, 0, v113, vcc
	global_load_dwordx4 v[196:199], v[112:113], off offset:2048
	s_waitcnt vmcnt(0)
	v_lshlrev_b32_e32 v112, 16, v196
	v_and_b32_e32 v113, 0xffff0000, v196
	v_pk_add_f32 v[112:113], v[112:113], v[102:103] op_sel_hi:[1,0] neg_lo:[0,1] neg_hi:[0,1]
	s_nop 0
	v_pk_mul_f32 v[112:113], v[108:109], v[112:113] op_sel_hi:[0,1]
	v_pk_fma_f32 v[112:113], v[92:93], v[112:113], v[96:97]
	s_nop 0
	v_cvt_pk_bf16_f32 v196, v112, v113
	v_lshlrev_b32_e32 v112, 16, v197
	v_and_b32_e32 v113, 0xffff0000, v197
	v_pk_add_f32 v[112:113], v[112:113], v[102:103] op_sel_hi:[1,0] neg_lo:[0,1] neg_hi:[0,1]
	s_nop 0
	v_pk_mul_f32 v[112:113], v[108:109], v[112:113] op_sel_hi:[0,1]
	v_pk_fma_f32 v[112:113], v[94:95], v[112:113], v[98:99]
	s_nop 0
	v_cvt_pk_bf16_f32 v197, v112, v113
	v_lshlrev_b32_e32 v112, 16, v198
	v_and_b32_e32 v113, 0xffff0000, v198
	v_pk_add_f32 v[112:113], v[112:113], v[102:103] op_sel_hi:[1,0] neg_lo:[0,1] neg_hi:[0,1]
	s_nop 0
	v_pk_mul_f32 v[112:113], v[108:109], v[112:113] op_sel_hi:[0,1]
	v_pk_fma_f32 v[112:113], v[84:85], v[112:113], v[88:89]
	s_nop 0
	v_cvt_pk_bf16_f32 v198, v112, v113
	v_lshlrev_b32_e32 v112, 16, v199
	v_and_b32_e32 v113, 0xffff0000, v199
	v_pk_add_f32 v[102:103], v[112:113], v[102:103] op_sel_hi:[1,0] neg_lo:[0,1] neg_hi:[0,1]
	s_nop 0
	v_pk_mul_f32 v[102:103], v[108:109], v[102:103] op_sel_hi:[0,1]
	v_pk_fma_f32 v[102:103], v[86:87], v[102:103], v[90:91]
	v_add_u32_e32 v108, 0x60, v185
	v_cvt_pk_bf16_f32 v199, v102, v103
	v_lshlrev_b32_e32 v102, 8, v114
	v_and_b32_e32 v102, 0xffffc000, v102
	v_add3_u32 v102, 0, v102, v116
	v_add3_u32 v102, v102, v189, v190
	ds_write_b128 v102, v[196:199]
	v_add_u32_e32 v102, s11, v108
	v_mad_i64_i32 v[100:101], s[0:1], v102, s14, v[100:101]
	v_lshl_add_u64 v[100:101], v[100:101], 0, v[110:111]
	v_add_co_u32_e32 v100, vcc, s4, v100
	s_cselect_b64 s[0:1], -1, 0
	s_nop 0
	v_addc_co_u32_e32 v101, vcc, 0, v101, vcc
	global_load_dwordx4 v[100:103], v[100:101], off offset:2048
	v_cmp_le_u32_e32 vcc, v183, v182
	s_mov_b64 s[4:5], -1
	s_waitcnt vmcnt(0)
; __device__ __forceinline__ unsigned cvt_pk_bf16(float lo, float hi) { f32x2_t v = {lo, hi}; bf16x2_t b = __builtin_convertvector(v, bf16x2_t); return __builtin_bit_cast(unsigned, b); }
; #define LAS __attribute__((address_space(3)))
; __device__ __forceinline__ void unit(const bf16_t* proj, const float* stats  , const float* lng, const float* lnb, const float* sw, const float* sb, bf16_t* Y2, int un, LAS unsigned char* lds) {
;     ...
;       for (int q = 0; q < 4; ++q) { const int s = sr + 32 * q, row = R0 + s; const u32x4 vv = *(const u32x4*)(proj + (size_t)row * NC + C_VC + ch);
;           const float mu = mus[q], rs = rss[q];
;           u32x4 w; w.x = pg8::cvt_pk_bf16((bflo(vv.x) - mu) * rs * g0[0] + b0[0], (bfhi(vv.x) - mu) * rs * g0[1] + b0[1]); w.y = pg8::cvt_pk_bf16((bflo(vv.y) - mu) * rs * g0[2] + b0[2], (bfhi(vv.y) - mu) * rs * g0[3] + b0[3]);
;           w.z = pg8::cvt_pk_bf16((bflo(vv.z) - mu) * rs * g1[0] + b1[0], (bfhi(vv.z) - mu) * rs * g1[1] + b1[1]); w.w = pg8::cvt_pk_bf16((bflo(vv.w) - mu) * rs * g1[2] + b1[2], (bfhi(vv.w) - mu) * rs * g1[3] + b1[3]);
;           *(LAS u32x4*)(lds + (s >> 6) * att::SHM_V + att::v_st(s & 63, sc)) = w; } }
;     __syncthreads();
;     att::f32x16 o0 = att::f32x16{}, o1 = att::f32x16{};
;     LAS const unsigned char* vb = lds + att::v_rd_base(lane);
; #pragma unroll
;     for (int st = 0; st < 2; ++st) {
;         if (st * 64 > tb * 32 + 31) continue;
;         att::bf16x8 pa[4];
; #pragma unroll
;         for (int k = 0; k < 4; ++k) { const int s0 = st * 64 + 16 * k + hi * 8; const f32x4 w0 = wv[2 * (st * 4 + k)], w1 = wv[2 * (st * 4 + k) + 1];
;             float x[8] = {w0[0], w0[1], w0[2], w0[3], w1[0], w1[1], w1[2], w1[3]};
; #pragma unroll
;             for (int j = 0; j < 8; ++j) x[j] = (s0 + j <= t) ? x[j] : 0.f;
;             u32x4 p; p.x = pg8::cvt_pk_bf16(x[0], x[1]); p.y = pg8::cvt_pk_bf16(x[2], x[3]); p.z = pg8::cvt_pk_bf16(x[4], x[5]); p.w = pg8::cvt_pk_bf16(x[6], x[7]); pa[k] = __builtin_bit_cast(att::bf16x8, p); }
;         if (eh == 0) { att::pv_one<0>(o0, vb + st * att::SHM_V, pa[0], pa[1], pa[2], pa[3]); att::pv_one<1>(o1, vb + st * att::SHM_V, pa[0], pa[1], pa[2], pa[3]); }
;         else         { att::pv_one<2>(o0, vb + st * att::SHM_V, pa[0], pa[1], pa[2], pa[3]); att::pv_one<3>(o1, vb + st * att::SHM_V, pa[0], pa[1], pa[2], pa[3]); }
	v_lshlrev_b32_e32 v110, 16, v100
	v_and_b32_e32 v111, 0xffff0000, v100
	v_pk_add_f32 v[110:111], v[110:111], v[104:105] op_sel_hi:[1,0] neg_lo:[0,1] neg_hi:[0,1]
	v_cndmask_b32_e32 v32, 0, v32, vcc
	v_pk_mul_f32 v[110:111], v[106:107], v[110:111] op_sel_hi:[0,1]
	v_pk_fma_f32 v[92:93], v[92:93], v[110:111], v[96:97]
	v_lshlrev_b32_e32 v96, 16, v101
	v_and_b32_e32 v97, 0xffff0000, v101
	v_pk_add_f32 v[96:97], v[96:97], v[104:105] op_sel_hi:[1,0] neg_lo:[0,1] neg_hi:[0,1]
	v_cvt_pk_bf16_f32 v92, v92, v93
	v_pk_mul_f32 v[96:97], v[106:107], v[96:97] op_sel_hi:[0,1]
	v_pk_fma_f32 v[94:95], v[94:95], v[96:97], v[98:99]
	v_cmp_lt_u32_e32 vcc, v183, v182
	v_cvt_pk_bf16_f32 v93, v94, v95
	v_lshlrev_b32_e32 v94, 16, v102
	v_and_b32_e32 v95, 0xffff0000, v102
	v_pk_add_f32 v[94:95], v[94:95], v[104:105] op_sel_hi:[1,0] neg_lo:[0,1] neg_hi:[0,1]
	v_cndmask_b32_e32 v33, 0, v33, vcc
	v_pk_mul_f32 v[94:95], v[106:107], v[94:95] op_sel_hi:[0,1]
	v_pk_fma_f32 v[84:85], v[84:85], v[94:95], v[88:89]
	s_nop 0
	v_cvt_pk_bf16_f32 v94, v84, v85
	v_lshlrev_b32_e32 v84, 16, v103
	v_and_b32_e32 v85, 0xffff0000, v103
	v_pk_add_f32 v[84:85], v[84:85], v[104:105] op_sel_hi:[1,0] neg_lo:[0,1] neg_hi:[0,1]
	s_nop 0
	v_pk_mul_f32 v[84:85], v[106:107], v[84:85] op_sel_hi:[0,1]
	v_pk_fma_f32 v[84:85], v[86:87], v[84:85], v[90:91]
	v_and_b32_e32 v86, 0xc0, v186
	v_cvt_pk_bf16_f32 v95, v84, v85
	v_and_or_b32 v85, v108, 48, v187
	v_lshrrev_b32_e32 v85, 1, v85
	v_lshlrev_b32_e32 v84, 8, v108
	v_or_b32_e32 v85, v85, v188
	v_and_b32_e32 v84, 0xffffc000, v84
	v_lshlrev_b32_e32 v85, 9, v85
	v_add3_u32 v84, 0, v84, v85
	v_add3_u32 v84, v84, v189, v190
	ds_write_b128 v84, v[92:95]
	v_lshlrev_b32_e32 v84, 3, v184
	v_and_b32_e32 v85, 24, v84
	v_lshlrev_b32_e32 v87, 1, v176
	v_and_b32_e32 v87, 32, v87
	v_and_b32_e32 v84, 0x100, v84
	v_add3_u32 v85, 0, v85, v86
	v_add3_u32 v100, v85, v87, v84
	v_or_b32_e32 v84, 2, v183
	v_cmp_le_u32_e32 vcc, v84, v182
	v_or_b32_e32 v84, 3, v183
	s_waitcnt lgkmcnt(0)
	v_cndmask_b32_e32 v34, 0, v34, vcc
	v_cmp_le_u32_e32 vcc, v84, v182
	v_or_b32_e32 v84, 4, v183
	s_barrier
	v_cndmask_b32_e32 v35, 0, v35, vcc
	v_cmp_le_u32_e32 vcc, v84, v182
	v_or_b32_e32 v84, 5, v183
	v_cvt_pk_bf16_f32 v85, v34, v35
	v_cndmask_b32_e32 v28, 0, v28, vcc
	v_cmp_le_u32_e32 vcc, v84, v182
	v_or_b32_e32 v84, 6, v183
	s_nop 0
	v_cndmask_b32_e32 v29, 0, v29, vcc
	v_cmp_le_u32_e32 vcc, v84, v182
	v_or_b32_e32 v84, 7, v183
	v_cvt_pk_bf16_f32 v86, v28, v29
	v_cndmask_b32_e32 v30, 0, v30, vcc
	v_cmp_le_u32_e32 vcc, v84, v182
	v_or_b32_e32 v28, 16, v183
	v_cvt_pk_bf16_f32 v84, v32, v33
	v_cndmask_b32_e32 v31, 0, v31, vcc
	v_cmp_le_u32_e32 vcc, v28, v182
	v_or_b32_e32 v28, 17, v183
	v_cvt_pk_bf16_f32 v87, v30, v31
	v_cndmask_b32_e32 v24, 0, v24, vcc
	v_cmp_le_u32_e32 vcc, v28, v182
	v_or_b32_e32 v28, 18, v183
	s_nop 0
	v_cndmask_b32_e32 v25, 0, v25, vcc
	v_cmp_le_u32_e32 vcc, v28, v182
	v_or_b32_e32 v28, 19, v183
	v_cvt_pk_bf16_f32 v88, v24, v25
	v_cndmask_b32_e32 v26, 0, v26, vcc
	v_cmp_le_u32_e32 vcc, v28, v182
	v_or_b32_e32 v28, 20, v183
	s_nop 0
	v_cndmask_b32_e32 v27, 0, v27, vcc
	v_cmp_le_u32_e32 vcc, v28, v182
	v_or_b32_e32 v28, 21, v183
	v_cvt_pk_bf16_f32 v89, v26, v27
	v_cndmask_b32_e32 v20, 0, v20, vcc
	v_cmp_le_u32_e32 vcc, v28, v182
	v_or_b32_e32 v28, 22, v183
	s_nop 0
	v_cndmask_b32_e32 v21, 0, v21, vcc
	v_cmp_le_u32_e32 vcc, v28, v182
	v_or_b32_e32 v28, 23, v183
	v_cvt_pk_bf16_f32 v90, v20, v21
	v_cndmask_b32_e32 v22, 0, v22, vcc
	v_cmp_le_u32_e32 vcc, v28, v182
	v_or_b32_e32 v20, 32, v183
	s_nop 0
	v_cndmask_b32_e32 v23, 0, v23, vcc
	v_cmp_le_u32_e32 vcc, v20, v182
	v_or_b32_e32 v20, 33, v183
	v_cvt_pk_bf16_f32 v91, v22, v23
	v_cndmask_b32_e32 v16, 0, v16, vcc
	v_cmp_le_u32_e32 vcc, v20, v182
	v_or_b32_e32 v20, 34, v183
	s_nop 0
	v_cndmask_b32_e32 v17, 0, v17, vcc
	v_cmp_le_u32_e32 vcc, v20, v182
	v_or_b32_e32 v20, 35, v183
	v_cvt_pk_bf16_f32 v96, v16, v17
	v_cndmask_b32_e32 v18, 0, v18, vcc
	v_cmp_le_u32_e32 vcc, v20, v182
	v_or_b32_e32 v20, 36, v183
	s_nop 0
	v_cndmask_b32_e32 v19, 0, v19, vcc
	v_cmp_le_u32_e32 vcc, v20, v182
	v_or_b32_e32 v20, 37, v183
	v_cvt_pk_bf16_f32 v97, v18, v19
	v_cndmask_b32_e32 v12, 0, v12, vcc
	v_cmp_le_u32_e32 vcc, v20, v182
	v_or_b32_e32 v20, 38, v183
	s_nop 0
	v_cndmask_b32_e32 v13, 0, v13, vcc
	v_cmp_le_u32_e32 vcc, v20, v182
	v_or_b32_e32 v20, 39, v183
	v_cvt_pk_bf16_f32 v98, v12, v13
	v_cndmask_b32_e32 v14, 0, v14, vcc
	v_cmp_le_u32_e32 vcc, v20, v182
	v_or_b32_e32 v12, 48, v183
	s_nop 0
	v_cndmask_b32_e32 v15, 0, v15, vcc
	v_cmp_le_u32_e32 vcc, v12, v182
	v_or_b32_e32 v12, 49, v183
	v_cvt_pk_bf16_f32 v99, v14, v15
	v_cndmask_b32_e32 v8, 0, v8, vcc
	v_cmp_le_u32_e32 vcc, v12, v182
	v_or_b32_e32 v12, 50, v183
	s_nop 0
	v_cndmask_b32_e32 v9, 0, v9, vcc
	v_cmp_le_u32_e32 vcc, v12, v182
	v_or_b32_e32 v12, 51, v183
	v_cvt_pk_bf16_f32 v92, v8, v9
	v_cndmask_b32_e32 v10, 0, v10, vcc
	v_cmp_le_u32_e32 vcc, v12, v182
	v_or_b32_e32 v12, 52, v183
	s_nop 0
	v_cndmask_b32_e32 v11, 0, v11, vcc
	v_cmp_le_u32_e32 vcc, v12, v182
	v_or_b32_e32 v12, 53, v183
	v_cvt_pk_bf16_f32 v93, v10, v11
	v_cndmask_b32_e32 v4, 0, v4, vcc
	v_cmp_le_u32_e32 vcc, v12, v182
	v_or_b32_e32 v12, 54, v183
	s_nop 0
	v_cndmask_b32_e32 v5, 0, v5, vcc
	v_cmp_le_u32_e32 vcc, v12, v182
	v_or_b32_e32 v12, 55, v183
	v_cvt_pk_bf16_f32 v94, v4, v5
	v_cndmask_b32_e32 v6, 0, v6, vcc
	v_cmp_le_u32_e32 vcc, v12, v182
	s_nop 1
	v_cndmask_b32_e32 v7, 0, v7, vcc
	v_cvt_pk_bf16_f32 v95, v6, v7
	s_and_b64 vcc, exec, s[0:1]
	s_cbranch_vccz .LBB0_1379
	ds_read_b64_tr_b16 v[4:5], v100 offset:1024
	ds_read_b64_tr_b16 v[6:7], v100 offset:3072
	ds_read_b64_tr_b16 v[20:21], v100 offset:5120
	ds_read_b64_tr_b16 v[22:23], v100 offset:7168
	s_mov_b64 s[4:5], 0
	s_waitcnt lgkmcnt(2)
	v_mfma_f32_32x32x16_bf16 v[4:19], v[84:87], v[4:7], 0
	s_waitcnt lgkmcnt(0)
	v_mfma_f32_32x32x16_bf16 v[4:19], v[88:91], v[20:23], v[4:19]
	ds_read_b64_tr_b16 v[20:21], v100 offset:9216
	ds_read_b64_tr_b16 v[22:23], v100 offset:11264
	s_waitcnt lgkmcnt(0)
	v_mfma_f32_32x32x16_bf16 v[4:19], v[96:99], v[20:23], v[4:19]
	ds_read_b64_tr_b16 v[20:21], v100 offset:13312
	ds_read_b64_tr_b16 v[22:23], v100 offset:15360
	s_waitcnt lgkmcnt(0)
	v_mfma_f32_32x32x16_bf16 v[4:19], v[92:95], v[20:23], v[4:19]
	ds_read_b64_tr_b16 v[22:23], v100 offset:3584
	ds_read_b64_tr_b16 v[20:21], v100 offset:1536
	ds_read_b64_tr_b16 v[104:105], v100 offset:7680
	ds_read_b64_tr_b16 v[102:103], v100 offset:5632
	s_waitcnt lgkmcnt(2)
	v_mfma_f32_32x32x16_bf16 v[20:35], v[84:87], v[20:23], 0
	s_waitcnt lgkmcnt(0)
	v_mfma_f32_32x32x16_bf16 v[20:35], v[88:91], v[102:105], v[20:35]
	ds_read_b64_tr_b16 v[104:105], v100 offset:11776
	ds_read_b64_tr_b16 v[102:103], v100 offset:9728
	s_waitcnt lgkmcnt(0)
	v_mfma_f32_32x32x16_bf16 v[20:35], v[96:99], v[102:105], v[20:35]
	ds_read_b64_tr_b16 v[104:105], v100 offset:15872
	ds_read_b64_tr_b16 v[102:103], v100 offset:13824
	s_waitcnt lgkmcnt(0)
	v_mfma_f32_32x32x16_bf16 v[20:35], v[92:95], v[102:105], v[20:35]
